# speedup vs baseline: 1.0038x; 1.0038x over previous
.Lk1_flush:
	s_barrier
	s_add_u32 s20, s40, 0x0
	s_addc_u32 s21, s41, 0
	s_add_u32 s22, s20, 0x186a000
	s_addc_u32 s23, s21, 0
	s_add_u32 s24, s22, 0x186a000
	s_addc_u32 s25, s23, 0
	s_add_u32 s26, s24, 0x186a000
	s_addc_u32 s27, s25, 0
	global_store_dword v39, v56, s[20:21] sc1
	global_store_dword v39, v57, s[22:23] sc1
	global_store_dword v39, v58, s[24:25] sc1
	global_store_dword v39, v59, s[26:27] sc1
	global_store_dword v39, v60, s[20:21] offset:1024 sc1
	global_store_dword v39, v61, s[22:23] offset:1024 sc1
	global_store_dword v39, v62, s[24:25] offset:1024 sc1
	global_store_dword v39, v63, s[26:27] offset:1024 sc1
	global_store_dword v39, v64, s[20:21] offset:2048 sc1
	global_store_dword v39, v65, s[22:23] offset:2048 sc1
	global_store_dword v39, v66, s[24:25] offset:2048 sc1
	global_store_dword v39, v67, s[26:27] offset:2048 sc1
	global_store_dword v39, v68, s[20:21] offset:3072 sc1
	global_store_dword v39, v69, s[22:23] offset:3072 sc1
	global_store_dword v39, v70, s[24:25] offset:3072 sc1
	global_store_dword v39, v71, s[26:27] offset:3072 sc1
	s_add_u32 s20, s20, 0x1000
	s_addc_u32 s21, s21, 0
	s_add_u32 s22, s22, 0x1000
	s_addc_u32 s23, s23, 0
	s_add_u32 s24, s24, 0x1000
	s_addc_u32 s25, s25, 0
	s_add_u32 s26, s26, 0x1000
	s_addc_u32 s27, s27, 0
	global_store_dword v39, v72, s[20:21] sc1
	global_store_dword v39, v73, s[22:23] sc1
	global_store_dword v39, v74, s[24:25] sc1
	global_store_dword v39, v75, s[26:27] sc1
	global_store_dword v39, v76, s[20:21] offset:1024 sc1
	global_store_dword v39, v77, s[22:23] offset:1024 sc1
	global_store_dword v39, v78, s[24:25] offset:1024 sc1
	global_store_dword v39, v79, s[26:27] offset:1024 sc1
	global_store_dword v39, v80, s[20:21] offset:2048 sc1
	global_store_dword v39, v81, s[22:23] offset:2048 sc1
	global_store_dword v39, v82, s[24:25] offset:2048 sc1
	global_store_dword v39, v83, s[26:27] offset:2048 sc1
	global_store_dword v39, v84, s[20:21] offset:3072 sc1
	global_store_dword v39, v85, s[22:23] offset:3072 sc1
	global_store_dword v39, v86, s[24:25] offset:3072 sc1
	global_store_dword v39, v87, s[26:27] offset:3072 sc1
	s_add_u32 s20, s20, 0x1000
	s_addc_u32 s21, s21, 0
	s_add_u32 s22, s22, 0x1000
	s_addc_u32 s23, s23, 0
	s_add_u32 s24, s24, 0x1000
	s_addc_u32 s25, s25, 0
	s_add_u32 s26, s26, 0x1000
	s_addc_u32 s27, s27, 0
	global_store_dword v39, v88, s[20:21] sc1
	global_store_dword v39, v89, s[22:23] sc1
	global_store_dword v39, v90, s[24:25] sc1
	global_store_dword v39, v91, s[26:27] sc1
	global_store_dword v39, v92, s[20:21] offset:1024 sc1
	global_store_dword v39, v93, s[22:23] offset:1024 sc1
	global_store_dword v39, v94, s[24:25] offset:1024 sc1
	global_store_dword v39, v95, s[26:27] offset:1024 sc1
	global_store_dword v39, v96, s[20:21] offset:2048 sc1
	global_store_dword v39, v97, s[22:23] offset:2048 sc1
	global_store_dword v39, v98, s[24:25] offset:2048 sc1
	global_store_dword v39, v99, s[26:27] offset:2048 sc1
	global_store_dword v39, v100, s[20:21] offset:3072 sc1
	global_store_dword v39, v101, s[22:23] offset:3072 sc1
	global_store_dword v39, v102, s[24:25] offset:3072 sc1
	global_store_dword v39, v103, s[26:27] offset:3072 sc1
	s_add_u32 s20, s20, 0x1000
	s_addc_u32 s21, s21, 0
	s_add_u32 s22, s22, 0x1000
	s_addc_u32 s23, s23, 0
	s_add_u32 s24, s24, 0x1000
	s_addc_u32 s25, s25, 0
	s_add_u32 s26, s26, 0x1000
	s_addc_u32 s27, s27, 0
	global_store_dword v39, v104, s[20:21] sc1
	global_store_dword v39, v105, s[22:23] sc1
	global_store_dword v39, v106, s[24:25] sc1
	global_store_dword v39, v107, s[26:27] sc1
	global_store_dword v39, v108, s[20:21] offset:1024 sc1
	global_store_dword v39, v109, s[22:23] offset:1024 sc1
	global_store_dword v39, v110, s[24:25] offset:1024 sc1
	global_store_dword v39, v111, s[26:27] offset:1024 sc1
	global_store_dword v39, v112, s[20:21] offset:2048 sc1
	global_store_dword v39, v113, s[22:23] offset:2048 sc1
	global_store_dword v39, v114, s[24:25] offset:2048 sc1
	global_store_dword v39, v115, s[26:27] offset:2048 sc1
	global_store_dword v39, v116, s[20:21] offset:3072 sc1
	global_store_dword v39, v117, s[22:23] offset:3072 sc1
	global_store_dword v39, v118, s[24:25] offset:3072 sc1
	global_store_dword v39, v119, s[26:27] offset:3072 sc1
	s_add_u32 s20, s20, 0x1000
	s_addc_u32 s21, s21, 0
	s_add_u32 s22, s22, 0x1000
	s_addc_u32 s23, s23, 0
	s_add_u32 s24, s24, 0x1000
	s_addc_u32 s25, s25, 0
	s_add_u32 s26, s26, 0x1000
	s_addc_u32 s27, s27, 0
	global_store_dword v39, v120, s[20:21] sc1
	global_store_dword v39, v121, s[22:23] sc1
	global_store_dword v39, v122, s[24:25] sc1
	global_store_dword v39, v123, s[26:27] sc1
	global_store_dword v39, v124, s[20:21] offset:1024 sc1
	global_store_dword v39, v125, s[22:23] offset:1024 sc1
	global_store_dword v39, v126, s[24:25] offset:1024 sc1
	global_store_dword v39, v127, s[26:27] offset:1024 sc1
	global_store_dword v39, v36, s[20:21] offset:2048 sc1
	global_store_dword v39, v37, s[22:23] offset:2048 sc1
	global_store_dword v39, v45, s[24:25] offset:2048 sc1
	global_store_dword v39, v46, s[26:27] offset:2048 sc1
	global_store_dword v39, v53, s[20:21] offset:3072 sc1
	global_store_dword v39, v54, s[22:23] offset:3072 sc1
	global_store_dword v39, v55, s[24:25] offset:3072 sc1
	global_store_dword v39, v1, s[26:27] offset:3072 sc1
	v_mul_f32_e32 v40, 0x3c010204, v40
	v_and_b32_e32 v42, 63, v0
	v_lshlrev_b32_e32 v41, 5, v42
	s_add_u32 s15, s12, s14
	s_lshl_b32 s15, s15, 2
	s_add_u32 s8, s8, s15
	s_addc_u32 s9, s9, 0
	s_add_u32 s15, s29, 24
	v_cmp_gt_u32_e32 vcc, s15, v42
	s_and_saveexec_b64 s[38:39], vcc
	global_store_dword v41, v40, s[8:9]
	s_mov_b64 exec, s[38:39]
	s_lshl_b32 s15, s14, 12
	v_add_u32_e32 v41, s15, v34
	s_barrier
	ds_write_b128 v41, v[2:5]
	ds_write_b128 v41, v[6:9] offset:1024
	ds_write_b128 v41, v[10:13] offset:2048
	ds_write_b128 v41, v[14:17] offset:3072
	s_waitcnt lgkmcnt(0)
	s_barrier
	s_movk_i32 s15, 0x100
	v_cmp_gt_u32_e32 vcc, s15, v0
	s_and_saveexec_b64 s[38:39], vcc
	s_cbranch_execz .Lk1_end
	v_lshlrev_b32_e32 v16, 4, v0
	ds_read_b128 v[2:5], v16
	ds_read_b128 v[18:21], v16 offset:4096
	ds_read_b128 v[22:25], v16 offset:8192
	ds_read_b128 v[26:29], v16 offset:12288
	ds_read_b128 v[30:33], v16 offset:16384
	ds_read_b128 v[34:37], v16 offset:20480
	ds_read_b128 v[38:41], v16 offset:24576
	ds_read_b128 v[42:45], v16 offset:28672
	s_waitcnt lgkmcnt(6)
	v_pk_add_f32 v[2:3], v[2:3], v[18:19]
	v_pk_add_f32 v[4:5], v[4:5], v[20:21]
	s_waitcnt lgkmcnt(5)
	v_pk_add_f32 v[2:3], v[2:3], v[22:23]
	v_pk_add_f32 v[4:5], v[4:5], v[24:25]
	s_waitcnt lgkmcnt(4)
	v_pk_add_f32 v[2:3], v[2:3], v[26:27]
	v_pk_add_f32 v[4:5], v[4:5], v[28:29]
	s_waitcnt lgkmcnt(3)
	v_pk_add_f32 v[2:3], v[2:3], v[30:31]
	v_pk_add_f32 v[4:5], v[4:5], v[32:33]
	s_waitcnt lgkmcnt(2)
	v_pk_add_f32 v[2:3], v[2:3], v[34:35]
	v_pk_add_f32 v[4:5], v[4:5], v[36:37]
	s_waitcnt lgkmcnt(1)
	v_pk_add_f32 v[2:3], v[2:3], v[38:39]
	v_pk_add_f32 v[4:5], v[4:5], v[40:41]
	s_waitcnt lgkmcnt(0)
	v_pk_add_f32 v[2:3], v[2:3], v[42:43]
	v_pk_add_f32 v[4:5], v[4:5], v[44:45]
	s_lshl_b32 s15, s2, 12
	s_add_u32 s10, s10, s15
	s_addc_u32 s11, s11, 0
	global_store_dwordx4 v16, v[2:5], s[10:11]
